# P11 gate loads issued in pairs; WKV-prep (P8) items rebalanced 5:3 between the workgroups with a short / long P7 GEMM unit
# speedup vs baseline: 1.0036x; 1.0036x over previous
; #define LAS __attribute__((address_space(3)))
; __global__ void __launch_bounds__(NWAVES * 64, 2) mk_fwd(Args args) {
;     ...
;             const float* DECAY = P_DECAY; const bf16* ASIG = P_ASIG; const bf16* KP = P_KP; const bf16* RP = P_RP; const bf16* VP = P_VP; const bf16* KKs = P_KK;
;             unsigned char* REC = ws + WS_SBUF;
;             const __amdgpu_buffer_rsrc_t rs_w = __builtin_amdgcn_make_buffer_rsrc((void*)DECAY, 0, (int)((size_t)M * RW * 4), 0x00020000), rs_a = __builtin_amdgcn_make_buffer_rsrc((void*)ASIG, 0, (int)((size_t)M * RW * 2), 0x00020000),
;                 rs_q = __builtin_amdgcn_make_buffer_rsrc((void*)KKs, 0, (int)((size_t)M * RW * 2), 0x00020000), rs_k = __builtin_amdgcn_make_buffer_rsrc((void*)KP, 0, (int)((size_t)M * RW * 2), 0x00020000),
;                 rs_r = __builtin_amdgcn_make_buffer_rsrc((void*)RP, 0, (int)((size_t)M * RW * 2), 0x00020000);
;             LAS unsigned char* wl = lds + wave * 13824;
;             const int c16 = lane & 15, g4 = lane >> 4;
;             for (int it = gw; it < 8192; it += NGW) {
;                 const int h = it & 15, c = (it >> 4) & 127, b = it >> 11;
;                 int ln = lane; asm volatile("" : "+v"(ln));
;                 const size_t r0 = ((size_t)b * T + c * 16) * RW + h * 64;
;                 const float kac = (ka->in[24] + l * RW + h * 64)[ln];
.LBB0_745:
	s_add_i32 s0, s59, 9
	s_mov_b32 s1, s0
	s_cmp_gt_i32 s76, s1
	s_cselect_b64 s[2:3], -1, 0
	s_cmp_ge_i32 s1, s77
	s_cselect_b64 s[4:5], -1, 0
	s_or_b64 s[2:3], s[2:3], s[4:5]
	s_and_b64 vcc, exec, s[2:3]
	s_cbranch_vccnz .LBB0_751
	v_readlane_b32 s2, v254, 8
	s_waitcnt lgkmcnt(0)
	v_readlane_b32 s16, v254, 10
	v_readlane_b32 s3, v254, 9
	v_mbcnt_lo_u32_b32 v8, -1, 0
	v_mbcnt_hi_u32_b32 v8, -1, v8
	s_load_dword s17, s[2:3], 0x0
	s_mov_b32 s22, s84
	s_waitcnt lgkmcnt(0)
	s_movk_i32 s17, 128
	s_lshl_b32 s1, s22, 3
	v_readlane_b32 s18, v254, 0
	s_add_i32 s1, s1, s16
	s_movk_i32 s99, 0x2000
	s_cmp_lt_u32 s22, 128
	s_cselect_b32 s99, 0x1400, s99
	s_cbranch_scc0 .Lmy_p8hi
	s_branch .Lmy_p8lo
.Lmy_p8hi:
	s_add_i32 s1, s1, 0x1000
.Lmy_p8lo:
	v_readlane_b32 s19, v254, 1
	s_cmp_ge_i32 s1, s99
	s_cbranch_scc1 .LBB0_751
	s_load_dwordx2 s[26:27], s[18:19], 0x138
	s_lshl_b32 s2, s17, 3
	v_readlane_b32 s8, v254, 23
	v_readlane_b32 s12, v254, 27
	v_readlane_b32 s9, v254, 24
	s_waitcnt lgkmcnt(0)
	s_add_u32 s8, s26, 0x2df80000
	s_addc_u32 s3, s27, 0
	s_add_u32 s12, s26, 0x2ff80000
	s_addc_u32 s4, s27, 0
	s_add_u32 s20, s26, 0x29f80000
	s_addc_u32 s5, s27, 0
	s_add_u32 s24, s26, 0x27f80000
	s_addc_u32 s6, s27, 0
	v_readlane_b32 s11, v254, 26
	s_add_u32 s28, s26, 0x33f80000
	v_readlane_b32 s10, v254, 25
	s_mov_b32 s11, s83
	s_addc_u32 s7, s27, 0
	s_and_b32 s9, s3, 0xffff
	v_readlane_b32 s13, v254, 28
	v_readlane_b32 s14, v254, 29
	v_readlane_b32 s15, v254, 30
	v_writelane_b32 v254, s8, 23
	s_mul_i32 s3, s16, 0x3600
	s_and_b32 s13, s4, 0xffff
	v_writelane_b32 v254, s9, 24
	v_writelane_b32 v254, s10, 25
	v_writelane_b32 v254, s11, 26
	s_mov_b32 s15, s83
	s_and_b32 s29, s7, 0xffff
	s_and_b32 s21, s5, 0xffff
	s_and_b32 s25, s6, 0xffff
	s_add_i32 s3, s3, 0
	s_lshl_b32 s96, s58, 10
	s_mul_i32 s30, s1, 0x3000
	v_writelane_b32 v254, s12, 27
	v_ashrrev_i32_e32 v2, 2, v8
	s_mul_hi_i32 s23, s1, 0x3000
	s_add_u32 s26, s26, s30
	v_writelane_b32 v254, s13, 28
	v_and_b32_e32 v0, 15, v8
	v_and_b32_e32 v1, -16, v8
	s_movk_i32 s4, 0x90
	v_and_b32_e32 v3, -4, v2
	s_addc_u32 s23, s27, s23
	v_writelane_b32 v254, s14, 29
	v_mad_u32_u24 v1, v0, s4, v1
	v_cmp_lt_i32_e32 vcc, v0, v3
	v_cmp_gt_i32_e64 s[4:5], v0, v3
	s_waitcnt vmcnt(0)
	v_lshlrev_b32_e32 v4, 6, v3
	v_or_b32_e32 v5, 1, v3
	v_or_b32_e32 v3, 2, v3
	v_or_b32_e32 v2, 3, v2
	s_add_u32 s33, s26, 0x48780000
	v_writelane_b32 v254, s15, 30
	v_lshl_add_u32 v64, v0, 2, s3
	v_cmp_gt_i32_e64 s[6:7], v0, v5
	v_lshlrev_b32_e32 v5, 6, v5
	v_cmp_lt_i32_e64 s[8:9], v0, v3
	v_cmp_gt_i32_e64 s[10:11], v0, v3
	v_lshlrev_b32_e32 v3, 6, v3
	v_cmp_lt_i32_e64 s[12:13], v0, v2
	v_cmp_gt_i32_e64 s[14:15], v0, v2
	v_lshlrev_b32_e32 v0, 6, v2
	s_addc_u32 s36, s23, 0
	s_lshl_b32 s22, s22, 9
	s_lshl_b32 s16, s16, 6
	s_mul_i32 s37, s17, 0x18000
	s_add_i32 s38, s22, s16
	s_lshl_b32 s38, s1, 6
	s_lshl_b32 s39, s17, 9
	s_lshl_b64 s[34:35], s[96:97], 2
	v_add_u32_e32 v65, s3, v1
	v_add_u32_e32 v66, v64, v4
	v_add_u32_e32 v67, v64, v5
	v_add_u32_e32 v68, v64, v3
	v_add_u32_e32 v69, v64, v0
	s_branch .LBB0_749
.LBB0_748:
	s_or_b64 exec, exec, s[22:23]
	s_add_i32 s1, s1, s2
	s_add_u32 s33, s33, s37
	s_mul_hi_i32 s16, s2, 0x3000
	s_addc_u32 s36, s36, s16
	s_add_i32 s38, s38, s39
	s_cmp_lt_i32 s1, s99
	s_cbranch_scc0 .LBB0_751

;     __device__ __forceinline__ void operator()(AccMut acc, const Unit& u, int wr, int wc, int, int) const {
;     ...
;                     if (u.seg < 2) {
;                         const v4u ga = *(const v4u*)(gp + u.seg * D), gb = *(const v4u*)(gp + (u.seg + 1) * D);
;                         const float la[8] = {bflo(ga.x), bfhi(ga.x), bflo(ga.y), bfhi(ga.y), bflo(ga.z), bfhi(ga.z), bflo(ga.w), bfhi(ga.w)};
;                         const float lb[8] = {bflo(gb.x), bfhi(gb.x), bflo(gb.y), bfhi(gb.y), bflo(gb.z), bfhi(gb.z), bflo(gb.w), bfhi(gb.w)};
; #pragma unroll
;                         for (int j = 0; j < 8; ++j) { const float ea = __expf(-fminf(fmaxf(la[j], -30.f), 30.f)), eb = __expf(-fminf(fmaxf(lb[j], -30.f), 30.f)); sc[j] = (1.0f + eb) * __builtin_amdgcn_rcpf(1.0f + ea); }
.LBB0_916:
	s_andn2_b64 vcc, exec, s[6:7]
	s_cbranch_vccnz .LBB0_918
	s_lshl_b32 s96, s50, 12
	v_lshl_add_u64 v[4:5], v[152:153], 0, s[96:97]
	global_load_dwordx4 v[0:3], v[4:5], off
	v_add_co_u32_e32 v4, vcc, 0x1000, v4
	s_nop 1
	v_addc_co_u32_e32 v5, vcc, 0, v5, vcc
	global_load_dwordx4 v[4:7], v[4:5], off
	s_waitcnt vmcnt(1)
	v_lshlrev_b32_e32 v8, 16, v0
	v_lshlrev_b32_e32 v152, 16, v1
	v_and_b32_e32 v0, 0xffff0000, v0
	v_and_b32_e32 v1, 0xffff0000, v1
	v_lshlrev_b32_e32 v153, 16, v2
	v_lshlrev_b32_e32 v155, 16, v3
	v_and_b32_e32 v165, 0xffff0000, v3
	v_max_f32_e32 v3, v8, v8
	v_max_f32_e32 v8, v152, v152
	v_max_f32_e32 v0, v0, v0
	v_max_f32_e32 v1, v1, v1
	v_max_f32_e32 v152, v153, v153
	v_max_f32_e32 v153, v155, v155
	v_med3_f32 v8, v8, s54, v223
	v_med3_f32 v3, v3, s54, v223
	v_med3_f32 v0, v0, s54, v223
	v_med3_f32 v1, v1, s54, v223
	v_med3_f32 v153, v153, s54, v223
	v_mul_f32_e32 v8, 0xbfb8aa3b, v8
	v_and_b32_e32 v2, 0xffff0000, v2
	v_mul_f32_e32 v3, 0xbfb8aa3b, v3
	v_mul_f32_e32 v0, 0xbfb8aa3b, v0
	v_mul_f32_e32 v1, 0xbfb8aa3b, v1
	v_mul_f32_e32 v153, 0xbfb8aa3b, v153
	v_exp_f32_e32 v8, v8
	v_max_f32_e32 v2, v2, v2
	v_exp_f32_e32 v161, v3
	v_exp_f32_e32 v164, v153
	v_med3_f32 v2, v2, s54, v223
	v_mul_f32_e32 v2, 0xbfb8aa3b, v2
	v_add_f32_e32 v8, 1.0, v8
	v_med3_f32 v152, v152, s54, v223
	v_mul_f32_e32 v152, 0xbfb8aa3b, v152
	v_exp_f32_e32 v152, v152
	s_waitcnt vmcnt(0)
	v_lshlrev_b32_e32 v155, 16, v4
	v_and_b32_e32 v4, 0xffff0000, v4
	v_lshlrev_b32_e32 v158, 16, v5
	v_max_f32_e32 v155, v155, v155
	v_max_f32_e32 v4, v4, v4
	v_max_f32_e32 v158, v158, v158
	v_and_b32_e32 v5, 0xffff0000, v5
	v_med3_f32 v3, v155, s54, v223
	v_exp_f32_e32 v155, v0
	v_med3_f32 v0, v4, s54, v223
	v_med3_f32 v4, v158, s54, v223
	v_exp_f32_e32 v158, v1
	v_lshlrev_b32_e32 v159, 16, v6
	v_and_b32_e32 v6, 0xffff0000, v6
	v_lshlrev_b32_e32 v160, 16, v7
	v_max_f32_e32 v5, v5, v5
	v_max_f32_e32 v159, v159, v159
	v_max_f32_e32 v6, v6, v6
	v_max_f32_e32 v160, v160, v160
	v_med3_f32 v1, v5, s54, v223
	v_med3_f32 v5, v159, s54, v223
	v_exp_f32_e32 v159, v2
	v_med3_f32 v2, v6, s54, v223
	v_med3_f32 v6, v160, s54, v223
	v_mul_f32_e32 v3, 0xbfb8aa3b, v3
	v_mul_f32_e32 v160, 0xbfb8aa3b, v1
	v_mul_f32_e32 v153, 0xbfb8aa3b, v0
	v_exp_f32_e32 v0, v3
	v_exp_f32_e32 v3, v160
	v_add_f32_e32 v160, 1.0, v158
	v_rcp_f32_e32 v158, v8
	v_add_f32_e32 v8, 1.0, v164
	v_rcp_f32_e32 v164, v8
	v_max_f32_e32 v8, v165, v165
	v_med3_f32 v8, v8, s54, v223
	v_mul_f32_e32 v8, 0xbfb8aa3b, v8
	v_and_b32_e32 v7, 0xffff0000, v7
	v_exp_f32_e32 v8, v8
	v_max_f32_e32 v7, v7, v7
	v_med3_f32 v7, v7, s54, v223
	v_mul_f32_e32 v4, 0xbfb8aa3b, v4
	v_mul_f32_e32 v5, 0xbfb8aa3b, v5
	v_mul_f32_e32 v166, 0xbfb8aa3b, v2
	v_mul_f32_e32 v6, 0xbfb8aa3b, v6
	v_mul_f32_e32 v7, 0xbfb8aa3b, v7
	v_exp_f32_e32 v1, v153
	v_exp_f32_e32 v2, v4
	v_exp_f32_e32 v4, v5
	v_exp_f32_e32 v5, v166
	v_add_f32_e32 v153, 1.0, v161
	v_add_f32_e32 v155, 1.0, v155
	v_add_f32_e32 v161, 1.0, v152
	v_add_f32_e32 v166, 1.0, v159
	v_exp_f32_e32 v6, v6
	v_exp_f32_e32 v7, v7
	v_add_f32_e32 v8, 1.0, v8
	v_rcp_f32_e32 v152, v153
	v_rcp_f32_e32 v153, v155
	v_rcp_f32_e32 v159, v160
	v_rcp_f32_e32 v160, v161
	v_rcp_f32_e32 v161, v166
	v_rcp_f32_e32 v165, v8
	v_pk_add_f32 v[0:1], v[0:1], 1.0 op_sel_hi:[1,0]
	v_pk_add_f32 v[2:3], v[2:3], 1.0 op_sel_hi:[1,0]
	v_pk_add_f32 v[4:5], v[4:5], 1.0 op_sel_hi:[1,0]
	v_pk_add_f32 v[6:7], v[6:7], 1.0 op_sel_hi:[1,0]
	v_pk_mul_f32 v[4:5], v[4:5], v[160:161]
	v_pk_mul_f32 v[6:7], v[6:7], v[164:165]
	v_pk_mul_f32 v[2:3], v[2:3], v[158:159]
	v_pk_mul_f32 v[0:1], v[0:1], v[152:153]

;     __device__ __forceinline__ void operator()(AccMut acc, const Unit& u, int wr, int wc, int, int) const {
;     ...
;                     if (u.seg < 2) {
;                         const v4u ga = *(const v4u*)(gp + u.seg * D), gb = *(const v4u*)(gp + (u.seg + 1) * D);
;                         const float la[8] = {bflo(ga.x), bfhi(ga.x), bflo(ga.y), bfhi(ga.y), bflo(ga.z), bfhi(ga.z), bflo(ga.w), bfhi(ga.w)};
;                         const float lb[8] = {bflo(gb.x), bfhi(gb.x), bflo(gb.y), bfhi(gb.y), bflo(gb.z), bfhi(gb.z), bflo(gb.w), bfhi(gb.w)};
; #pragma unroll
;                         for (int j = 0; j < 8; ++j) { const float ea = __expf(-fminf(fmaxf(la[j], -30.f), 30.f)), eb = __expf(-fminf(fmaxf(lb[j], -30.f), 30.f)); sc[j] = (1.0f + eb) * __builtin_amdgcn_rcpf(1.0f + ea); }
.LBB0_923:
	s_andn2_b64 vcc, exec, s[2:3]
	s_cbranch_vccnz .LBB0_925
	s_lshl_b32 s96, s50, 12
	v_lshl_add_u64 v[0:1], v[156:157], 0, s[96:97]
	v_lshl_add_u64 v[4:5], v[152:153], 1, v[0:1]
	global_load_dwordx4 v[0:3], v[4:5], off
	v_add_co_u32_e32 v4, vcc, 0x1000, v4
	s_nop 1
	v_addc_co_u32_e32 v5, vcc, 0, v5, vcc
	global_load_dwordx4 v[4:7], v[4:5], off
	s_waitcnt vmcnt(1)
	v_lshlrev_b32_e32 v8, 16, v0
	v_lshlrev_b32_e32 v155, 16, v1
	v_and_b32_e32 v0, 0xffff0000, v0
	v_and_b32_e32 v1, 0xffff0000, v1
	v_lshlrev_b32_e32 v156, 16, v2
	v_lshlrev_b32_e32 v157, 16, v3
	v_and_b32_e32 v167, 0xffff0000, v3
	v_max_f32_e32 v3, v8, v8
	v_max_f32_e32 v8, v155, v155
	v_max_f32_e32 v0, v0, v0
	v_max_f32_e32 v1, v1, v1
	v_max_f32_e32 v155, v156, v156
	v_max_f32_e32 v156, v157, v157
	v_med3_f32 v8, v8, s54, v223
	v_med3_f32 v3, v3, s54, v223
	v_med3_f32 v0, v0, s54, v223
	v_med3_f32 v1, v1, s54, v223
	v_med3_f32 v156, v156, s54, v223
	v_mul_f32_e32 v8, 0xbfb8aa3b, v8
	v_and_b32_e32 v2, 0xffff0000, v2
	v_mul_f32_e32 v3, 0xbfb8aa3b, v3
	v_mul_f32_e32 v0, 0xbfb8aa3b, v0
	v_mul_f32_e32 v1, 0xbfb8aa3b, v1
	v_mul_f32_e32 v156, 0xbfb8aa3b, v156
	v_exp_f32_e32 v8, v8
	v_max_f32_e32 v2, v2, v2
	v_exp_f32_e32 v165, v3
	v_exp_f32_e32 v166, v156
	v_med3_f32 v2, v2, s54, v223
	v_mul_f32_e32 v2, 0xbfb8aa3b, v2
	v_add_f32_e32 v8, 1.0, v8
	v_med3_f32 v155, v155, s54, v223
	v_mul_f32_e32 v155, 0xbfb8aa3b, v155
	v_exp_f32_e32 v155, v155
	s_waitcnt vmcnt(0)
	v_lshlrev_b32_e32 v157, 16, v4
	v_and_b32_e32 v4, 0xffff0000, v4
	v_lshlrev_b32_e32 v160, 16, v5
	v_max_f32_e32 v157, v157, v157
	v_max_f32_e32 v4, v4, v4
	v_max_f32_e32 v160, v160, v160
	v_and_b32_e32 v5, 0xffff0000, v5
	v_med3_f32 v3, v157, s54, v223
	v_exp_f32_e32 v157, v0
	v_med3_f32 v0, v4, s54, v223
	v_med3_f32 v4, v160, s54, v223
	v_exp_f32_e32 v160, v1
	v_lshlrev_b32_e32 v161, 16, v6
	v_and_b32_e32 v6, 0xffff0000, v6
	v_lshlrev_b32_e32 v164, 16, v7
	v_max_f32_e32 v5, v5, v5
	v_max_f32_e32 v161, v161, v161
	v_max_f32_e32 v6, v6, v6
	v_max_f32_e32 v164, v164, v164
	v_med3_f32 v1, v5, s54, v223
	v_med3_f32 v5, v161, s54, v223
	v_exp_f32_e32 v161, v2
	v_med3_f32 v2, v6, s54, v223
	v_med3_f32 v6, v164, s54, v223
	v_mul_f32_e32 v3, 0xbfb8aa3b, v3
	v_mul_f32_e32 v164, 0xbfb8aa3b, v1
	v_mul_f32_e32 v156, 0xbfb8aa3b, v0
	v_exp_f32_e32 v0, v3
	v_exp_f32_e32 v3, v164
	v_add_f32_e32 v164, 1.0, v160
	v_rcp_f32_e32 v160, v8
	v_add_f32_e32 v8, 1.0, v166
	v_rcp_f32_e32 v166, v8
	v_max_f32_e32 v8, v167, v167
	v_med3_f32 v8, v8, s54, v223
	v_mul_f32_e32 v8, 0xbfb8aa3b, v8
	v_and_b32_e32 v7, 0xffff0000, v7
	v_exp_f32_e32 v8, v8
	v_max_f32_e32 v7, v7, v7
	v_med3_f32 v7, v7, s54, v223
	v_mul_f32_e32 v4, 0xbfb8aa3b, v4
	v_mul_f32_e32 v5, 0xbfb8aa3b, v5
	v_mul_f32_e32 v168, 0xbfb8aa3b, v2
	v_mul_f32_e32 v6, 0xbfb8aa3b, v6
	v_mul_f32_e32 v7, 0xbfb8aa3b, v7
	v_exp_f32_e32 v1, v156
	v_exp_f32_e32 v2, v4
	v_exp_f32_e32 v4, v5
	v_exp_f32_e32 v5, v168
	v_add_f32_e32 v156, 1.0, v165
	v_add_f32_e32 v157, 1.0, v157
	v_add_f32_e32 v155, 1.0, v155
	v_add_f32_e32 v165, 1.0, v161
	v_exp_f32_e32 v6, v6
	v_exp_f32_e32 v7, v7
	v_add_f32_e32 v8, 1.0, v8
	v_rcp_f32_e32 v156, v156
	v_rcp_f32_e32 v157, v157
	v_rcp_f32_e32 v161, v164
	v_rcp_f32_e32 v164, v155
	v_rcp_f32_e32 v165, v165
	v_rcp_f32_e32 v167, v8
	v_pk_add_f32 v[0:1], v[0:1], 1.0 op_sel_hi:[1,0]
	v_pk_add_f32 v[2:3], v[2:3], 1.0 op_sel_hi:[1,0]
	v_pk_add_f32 v[4:5], v[4:5], 1.0 op_sel_hi:[1,0]
	v_pk_add_f32 v[6:7], v[6:7], 1.0 op_sel_hi:[1,0]
	v_pk_mul_f32 v[4:5], v[4:5], v[164:165]
	v_pk_mul_f32 v[6:7], v[6:7], v[166:167]
	v_pk_mul_f32 v[2:3], v[2:3], v[160:161]
	v_pk_mul_f32 v[0:1], v[0:1], v[156:157]

;     __device__ __forceinline__ void operator()(AccMut acc, const Unit& u, int wr, int wc, int, int) const {
;     ...
;                     if (u.seg < 2) {
;                         const v4u ga = *(const v4u*)(gp + u.seg * D), gb = *(const v4u*)(gp + (u.seg + 1) * D);
;                         const float la[8] = {bflo(ga.x), bfhi(ga.x), bflo(ga.y), bfhi(ga.y), bflo(ga.z), bfhi(ga.z), bflo(ga.w), bfhi(ga.w)};
;                         const float lb[8] = {bflo(gb.x), bfhi(gb.x), bflo(gb.y), bfhi(gb.y), bflo(gb.z), bfhi(gb.z), bflo(gb.w), bfhi(gb.w)};
; #pragma unroll
;                         for (int j = 0; j < 8; ++j) { const float ea = __expf(-fminf(fmaxf(la[j], -30.f), 30.f)), eb = __expf(-fminf(fmaxf(lb[j], -30.f), 30.f)); sc[j] = (1.0f + eb) * __builtin_amdgcn_rcpf(1.0f + ea); }
.LBB0_930:
	s_andn2_b64 vcc, exec, s[2:3]
	s_cbranch_vccnz .LBB0_932
	s_lshl_b32 s96, s50, 12
	v_lshl_add_u64 v[4:5], v[160:161], 0, s[96:97]
	global_load_dwordx4 v[0:3], v[4:5], off
	v_add_co_u32_e32 v4, vcc, 0x1000, v4
	s_nop 1
	v_addc_co_u32_e32 v5, vcc, 0, v5, vcc
	global_load_dwordx4 v[4:7], v[4:5], off
	s_waitcnt vmcnt(1)
	v_lshlrev_b32_e32 v8, 16, v0
	v_lshlrev_b32_e32 v155, 16, v1
	v_and_b32_e32 v0, 0xffff0000, v0
	v_and_b32_e32 v1, 0xffff0000, v1
	v_lshlrev_b32_e32 v159, 16, v2
	v_and_b32_e32 v2, 0xffff0000, v2
	v_lshlrev_b32_e32 v160, 16, v3
	v_and_b32_e32 v169, 0xffff0000, v3
	v_max_f32_e32 v3, v8, v8
	v_max_f32_e32 v8, v155, v155
	v_max_f32_e32 v0, v0, v0
	v_max_f32_e32 v1, v1, v1
	v_max_f32_e32 v155, v159, v159
	v_max_f32_e32 v2, v2, v2
	v_max_f32_e32 v159, v160, v160
	v_med3_f32 v8, v8, s54, v223
	v_med3_f32 v3, v3, s54, v223
	v_med3_f32 v0, v0, s54, v223
	v_med3_f32 v1, v1, s54, v223
	v_med3_f32 v2, v2, s54, v223
	v_med3_f32 v159, v159, s54, v223
	v_mul_f32_e32 v8, 0xbfb8aa3b, v8
	v_mul_f32_e32 v3, 0xbfb8aa3b, v3
	v_mul_f32_e32 v0, 0xbfb8aa3b, v0
	v_mul_f32_e32 v1, 0xbfb8aa3b, v1
	v_mul_f32_e32 v2, 0xbfb8aa3b, v2
	v_mul_f32_e32 v159, 0xbfb8aa3b, v159
	v_exp_f32_e32 v8, v8
	v_exp_f32_e32 v166, v3
	v_exp_f32_e32 v159, v159
	v_med3_f32 v155, v155, s54, v223
	v_add_f32_e32 v8, 1.0, v8
	v_mul_f32_e32 v155, 0xbfb8aa3b, v155
	v_exp_f32_e32 v155, v155
	s_waitcnt vmcnt(0)
	v_lshlrev_b32_e32 v160, 16, v4
	v_and_b32_e32 v4, 0xffff0000, v4
	v_lshlrev_b32_e32 v161, 16, v5
	v_and_b32_e32 v5, 0xffff0000, v5
	v_lshlrev_b32_e32 v164, 16, v6
	v_max_f32_e32 v160, v160, v160
	v_max_f32_e32 v4, v4, v4
	v_max_f32_e32 v161, v161, v161
	v_max_f32_e32 v5, v5, v5
	v_max_f32_e32 v164, v164, v164
	v_and_b32_e32 v6, 0xffff0000, v6
	v_med3_f32 v3, v160, s54, v223
	v_exp_f32_e32 v160, v0
	v_med3_f32 v0, v4, s54, v223
	v_med3_f32 v4, v161, s54, v223
	v_exp_f32_e32 v161, v1
	v_med3_f32 v1, v5, s54, v223
	v_med3_f32 v5, v164, s54, v223
	v_exp_f32_e32 v164, v2
	v_lshlrev_b32_e32 v165, 16, v7
	v_max_f32_e32 v6, v6, v6
	v_max_f32_e32 v165, v165, v165
	v_med3_f32 v2, v6, s54, v223
	v_med3_f32 v6, v165, s54, v223
	v_mul_f32_e32 v3, 0xbfb8aa3b, v3
	v_mul_f32_e32 v165, 0xbfb8aa3b, v0
	v_mul_f32_e32 v4, 0xbfb8aa3b, v4
	v_mul_f32_e32 v167, 0xbfb8aa3b, v1
	v_mul_f32_e32 v5, 0xbfb8aa3b, v5
	v_mul_f32_e32 v168, 0xbfb8aa3b, v2
	v_exp_f32_e32 v0, v3
	v_exp_f32_e32 v1, v165
	v_exp_f32_e32 v2, v4
	v_exp_f32_e32 v3, v167
	v_exp_f32_e32 v4, v5
	v_exp_f32_e32 v5, v168
	v_add_f32_e32 v165, 1.0, v166
	v_add_f32_e32 v167, 1.0, v161
	v_add_f32_e32 v168, 1.0, v164
	v_rcp_f32_e32 v164, v8
	v_add_f32_e32 v8, 1.0, v159
	v_add_f32_e32 v166, 1.0, v160
	v_rcp_f32_e32 v160, v165
	v_rcp_f32_e32 v165, v167
	v_rcp_f32_e32 v167, v168
	v_rcp_f32_e32 v168, v8
	v_max_f32_e32 v8, v169, v169
	v_med3_f32 v8, v8, s54, v223
	v_mul_f32_e32 v8, 0xbfb8aa3b, v8
	v_and_b32_e32 v7, 0xffff0000, v7
	v_exp_f32_e32 v8, v8
	v_max_f32_e32 v7, v7, v7
	v_med3_f32 v7, v7, s54, v223
	v_mul_f32_e32 v6, 0xbfb8aa3b, v6
	v_mul_f32_e32 v7, 0xbfb8aa3b, v7
	v_add_f32_e32 v155, 1.0, v155
	v_exp_f32_e32 v6, v6
	v_exp_f32_e32 v7, v7
	v_add_f32_e32 v8, 1.0, v8
	v_rcp_f32_e32 v161, v166
	v_rcp_f32_e32 v166, v155
	v_rcp_f32_e32 v169, v8
	v_pk_add_f32 v[0:1], v[0:1], 1.0 op_sel_hi:[1,0]
	v_pk_add_f32 v[2:3], v[2:3], 1.0 op_sel_hi:[1,0]
	v_pk_add_f32 v[4:5], v[4:5], 1.0 op_sel_hi:[1,0]
	v_pk_add_f32 v[6:7], v[6:7], 1.0 op_sel_hi:[1,0]
	v_pk_mul_f32 v[4:5], v[4:5], v[166:167]
	v_pk_mul_f32 v[6:7], v[6:7], v[168:169]
	v_pk_mul_f32 v[2:3], v[2:3], v[164:165]
	v_pk_mul_f32 v[0:1], v[0:1], v[160:161]

;     __device__ __forceinline__ void operator()(AccMut acc, const Unit& u, int wr, int wc, int, int) const {
;     ...
;                     if (u.seg < 2) {
;                         const v4u ga = *(const v4u*)(gp + u.seg * D), gb = *(const v4u*)(gp + (u.seg + 1) * D);
;                         const float la[8] = {bflo(ga.x), bfhi(ga.x), bflo(ga.y), bfhi(ga.y), bflo(ga.z), bfhi(ga.z), bflo(ga.w), bfhi(ga.w)};
;                         const float lb[8] = {bflo(gb.x), bfhi(gb.x), bflo(gb.y), bfhi(gb.y), bflo(gb.z), bfhi(gb.z), bflo(gb.w), bfhi(gb.w)};
; #pragma unroll
;                         for (int j = 0; j < 8; ++j) { const float ea = __expf(-fminf(fmaxf(la[j], -30.f), 30.f)), eb = __expf(-fminf(fmaxf(lb[j], -30.f), 30.f)); sc[j] = (1.0f + eb) * __builtin_amdgcn_rcpf(1.0f + ea); }
.LBB0_1008:
	s_andn2_b64 vcc, exec, s[2:3]
	s_cbranch_vccnz .LBB0_1010
	s_lshl_b32 s96, s50, 12
	v_lshl_add_u64 v[4:5], v[158:159], 0, s[96:97]
	global_load_dwordx4 v[0:3], v[4:5], off
	v_add_co_u32_e32 v4, vcc, 0x1000, v4
	s_nop 1
	v_addc_co_u32_e32 v5, vcc, 0, v5, vcc
	global_load_dwordx4 v[4:7], v[4:5], off
	s_waitcnt vmcnt(1)
	v_lshlrev_b32_e32 v8, 16, v0
	v_lshlrev_b32_e32 v157, 16, v1
	v_and_b32_e32 v0, 0xffff0000, v0
	v_and_b32_e32 v1, 0xffff0000, v1
	v_lshlrev_b32_e32 v158, 16, v2
	v_lshlrev_b32_e32 v159, 16, v3
	v_and_b32_e32 v167, 0xffff0000, v3
	v_max_f32_e32 v3, v8, v8
	v_max_f32_e32 v8, v157, v157
	v_max_f32_e32 v0, v0, v0
	v_max_f32_e32 v1, v1, v1
	v_max_f32_e32 v157, v158, v158
	v_max_f32_e32 v158, v159, v159
	v_med3_f32 v8, v8, s54, v223
	v_med3_f32 v3, v3, s54, v223
	v_med3_f32 v0, v0, s54, v223
	v_med3_f32 v1, v1, s54, v223
	v_med3_f32 v158, v158, s54, v223
	v_mul_f32_e32 v8, 0xbfb8aa3b, v8
	v_and_b32_e32 v2, 0xffff0000, v2
	v_mul_f32_e32 v3, 0xbfb8aa3b, v3
	v_mul_f32_e32 v0, 0xbfb8aa3b, v0
	v_mul_f32_e32 v1, 0xbfb8aa3b, v1
	v_mul_f32_e32 v158, 0xbfb8aa3b, v158
	v_exp_f32_e32 v8, v8
	v_max_f32_e32 v2, v2, v2
	v_exp_f32_e32 v165, v3
	v_exp_f32_e32 v166, v158
	v_med3_f32 v2, v2, s54, v223
	v_mul_f32_e32 v2, 0xbfb8aa3b, v2
	v_add_f32_e32 v8, 1.0, v8
	v_med3_f32 v157, v157, s54, v223
	v_mul_f32_e32 v157, 0xbfb8aa3b, v157
	v_exp_f32_e32 v157, v157
	s_waitcnt vmcnt(0)
	v_lshlrev_b32_e32 v159, 16, v4
	v_and_b32_e32 v4, 0xffff0000, v4
	v_lshlrev_b32_e32 v160, 16, v5
	v_max_f32_e32 v159, v159, v159
	v_max_f32_e32 v4, v4, v4
	v_max_f32_e32 v160, v160, v160
	v_and_b32_e32 v5, 0xffff0000, v5
	v_med3_f32 v3, v159, s54, v223
	v_exp_f32_e32 v159, v0
	v_med3_f32 v0, v4, s54, v223
	v_med3_f32 v4, v160, s54, v223
	v_exp_f32_e32 v160, v1
	v_lshlrev_b32_e32 v161, 16, v6
	v_and_b32_e32 v6, 0xffff0000, v6
	v_lshlrev_b32_e32 v164, 16, v7
	v_max_f32_e32 v5, v5, v5
	v_max_f32_e32 v161, v161, v161
	v_max_f32_e32 v6, v6, v6
	v_max_f32_e32 v164, v164, v164
	v_med3_f32 v1, v5, s54, v223
	v_med3_f32 v5, v161, s54, v223
	v_exp_f32_e32 v161, v2
	v_med3_f32 v2, v6, s54, v223
	v_med3_f32 v6, v164, s54, v223
	v_mul_f32_e32 v3, 0xbfb8aa3b, v3
	v_mul_f32_e32 v164, 0xbfb8aa3b, v1
	v_mul_f32_e32 v158, 0xbfb8aa3b, v0
	v_exp_f32_e32 v0, v3
	v_exp_f32_e32 v3, v164
	v_add_f32_e32 v164, 1.0, v160
	v_rcp_f32_e32 v160, v8
	v_add_f32_e32 v8, 1.0, v166
	v_rcp_f32_e32 v166, v8
	v_max_f32_e32 v8, v167, v167
	v_med3_f32 v8, v8, s54, v223
	v_mul_f32_e32 v8, 0xbfb8aa3b, v8
	v_and_b32_e32 v7, 0xffff0000, v7
	v_exp_f32_e32 v8, v8
	v_max_f32_e32 v7, v7, v7
	v_med3_f32 v7, v7, s54, v223
	v_mul_f32_e32 v4, 0xbfb8aa3b, v4
	v_mul_f32_e32 v5, 0xbfb8aa3b, v5
	v_mul_f32_e32 v168, 0xbfb8aa3b, v2
	v_mul_f32_e32 v6, 0xbfb8aa3b, v6
	v_mul_f32_e32 v7, 0xbfb8aa3b, v7
	v_exp_f32_e32 v1, v158
	v_exp_f32_e32 v2, v4
	v_exp_f32_e32 v4, v5
	v_exp_f32_e32 v5, v168
	v_add_f32_e32 v158, 1.0, v165
	v_add_f32_e32 v159, 1.0, v159
	v_add_f32_e32 v157, 1.0, v157
	v_add_f32_e32 v165, 1.0, v161
	v_exp_f32_e32 v6, v6
	v_exp_f32_e32 v7, v7
	v_add_f32_e32 v8, 1.0, v8
	v_rcp_f32_e32 v158, v158
	v_rcp_f32_e32 v159, v159
	v_rcp_f32_e32 v161, v164
	v_rcp_f32_e32 v164, v157
	v_rcp_f32_e32 v165, v165
	v_rcp_f32_e32 v167, v8
	v_pk_add_f32 v[0:1], v[0:1], 1.0 op_sel_hi:[1,0]
	v_pk_add_f32 v[2:3], v[2:3], 1.0 op_sel_hi:[1,0]
	v_pk_add_f32 v[4:5], v[4:5], 1.0 op_sel_hi:[1,0]
	v_pk_add_f32 v[6:7], v[6:7], 1.0 op_sel_hi:[1,0]
	v_pk_mul_f32 v[4:5], v[4:5], v[164:165]
	v_pk_mul_f32 v[6:7], v[6:7], v[166:167]
	v_pk_mul_f32 v[2:3], v[2:3], v[160:161]
	v_pk_mul_f32 v[0:1], v[0:1], v[158:159]

;     __device__ __forceinline__ void operator()(AccMut acc, const Unit& u, int wr, int wc, int, int) const {
;     ...
;                     if (u.seg < 2) {
;                         const v4u ga = *(const v4u*)(gp + u.seg * D), gb = *(const v4u*)(gp + (u.seg + 1) * D);
;                         const float la[8] = {bflo(ga.x), bfhi(ga.x), bflo(ga.y), bfhi(ga.y), bflo(ga.z), bfhi(ga.z), bflo(ga.w), bfhi(ga.w)};
;                         const float lb[8] = {bflo(gb.x), bfhi(gb.x), bflo(gb.y), bfhi(gb.y), bflo(gb.z), bfhi(gb.z), bflo(gb.w), bfhi(gb.w)};
; #pragma unroll
;                         for (int j = 0; j < 8; ++j) { const float ea = __expf(-fminf(fmaxf(la[j], -30.f), 30.f)), eb = __expf(-fminf(fmaxf(lb[j], -30.f), 30.f)); sc[j] = (1.0f + eb) * __builtin_amdgcn_rcpf(1.0f + ea); }
.LBB0_1014:
	s_andn2_b64 vcc, exec, s[2:3]
	s_cbranch_vccnz .LBB0_1016
	s_lshl_b32 s96, s50, 12
	v_lshl_add_u64 v[0:1], v[154:155], 0, s[96:97]
	v_lshl_add_u64 v[4:5], v[152:153], 1, v[0:1]
	global_load_dwordx4 v[0:3], v[4:5], off
	v_add_co_u32_e32 v4, vcc, 0x1000, v4
	s_nop 1
	v_addc_co_u32_e32 v5, vcc, 0, v5, vcc
	global_load_dwordx4 v[4:7], v[4:5], off
	s_waitcnt vmcnt(1)
	v_lshlrev_b32_e32 v8, 16, v0
	v_and_b32_e32 v0, 0xffff0000, v0
	v_lshlrev_b32_e32 v152, 16, v1
	v_and_b32_e32 v1, 0xffff0000, v1
	v_lshlrev_b32_e32 v153, 16, v2
	v_and_b32_e32 v2, 0xffff0000, v2
	v_lshlrev_b32_e32 v154, 16, v3
	v_and_b32_e32 v159, 0xffff0000, v3
	v_max_f32_e32 v3, v8, v8
	v_max_f32_e32 v0, v0, v0
	v_max_f32_e32 v8, v152, v152
	v_max_f32_e32 v1, v1, v1
	v_max_f32_e32 v152, v153, v153
	v_max_f32_e32 v2, v2, v2
	v_max_f32_e32 v153, v154, v154
	v_med3_f32 v3, v3, s54, v223
	v_med3_f32 v0, v0, s54, v223
	v_med3_f32 v8, v8, s54, v223
	v_med3_f32 v1, v1, s54, v223
	v_med3_f32 v152, v152, s54, v223
	v_med3_f32 v2, v2, s54, v223
	v_med3_f32 v153, v153, s54, v223
	v_mul_f32_e32 v3, 0xbfb8aa3b, v3
	v_mul_f32_e32 v0, 0xbfb8aa3b, v0
	v_mul_f32_e32 v8, 0xbfb8aa3b, v8
	v_mul_f32_e32 v1, 0xbfb8aa3b, v1
	v_mul_f32_e32 v152, 0xbfb8aa3b, v152
	v_mul_f32_e32 v2, 0xbfb8aa3b, v2
	v_mul_f32_e32 v153, 0xbfb8aa3b, v153
	v_exp_f32_e32 v158, v3
	v_exp_f32_e32 v8, v8
	v_exp_f32_e32 v152, v152
	v_exp_f32_e32 v160, v153
	v_add_f32_e32 v8, 1.0, v8
	s_waitcnt vmcnt(0)
	v_lshlrev_b32_e32 v154, 16, v4
	v_and_b32_e32 v4, 0xffff0000, v4
	v_lshlrev_b32_e32 v155, 16, v5
	v_and_b32_e32 v5, 0xffff0000, v5
	v_lshlrev_b32_e32 v156, 16, v6
	v_max_f32_e32 v154, v154, v154
	v_max_f32_e32 v4, v4, v4
	v_max_f32_e32 v155, v155, v155
	v_max_f32_e32 v5, v5, v5
	v_max_f32_e32 v156, v156, v156
	v_med3_f32 v3, v154, s54, v223
	v_exp_f32_e32 v154, v0
	v_med3_f32 v0, v4, s54, v223
	v_med3_f32 v4, v155, s54, v223
	v_exp_f32_e32 v155, v1
	v_med3_f32 v1, v5, s54, v223
	v_med3_f32 v5, v156, s54, v223
	v_exp_f32_e32 v156, v2
	v_and_b32_e32 v6, 0xffff0000, v6
	v_lshlrev_b32_e32 v157, 16, v7
	v_max_f32_e32 v6, v6, v6
	v_max_f32_e32 v157, v157, v157
	v_mul_f32_e32 v153, 0xbfb8aa3b, v0
	v_med3_f32 v2, v6, s54, v223
	v_med3_f32 v6, v157, s54, v223
	v_mul_f32_e32 v3, 0xbfb8aa3b, v3
	v_mul_f32_e32 v157, 0xbfb8aa3b, v1
	v_exp_f32_e32 v1, v153
	v_add_f32_e32 v153, 1.0, v158
	v_add_f32_e32 v154, 1.0, v154
	v_exp_f32_e32 v0, v3
	v_exp_f32_e32 v3, v157
	v_add_f32_e32 v157, 1.0, v152
	v_add_f32_e32 v158, 1.0, v156
	v_rcp_f32_e32 v152, v153
	v_rcp_f32_e32 v153, v154
	v_rcp_f32_e32 v154, v8
	v_add_f32_e32 v8, 1.0, v160
	v_rcp_f32_e32 v156, v157
	v_rcp_f32_e32 v157, v158
	v_rcp_f32_e32 v158, v8
	v_max_f32_e32 v8, v159, v159
	v_med3_f32 v8, v8, s54, v223
	v_mul_f32_e32 v8, 0xbfb8aa3b, v8
	v_and_b32_e32 v7, 0xffff0000, v7
	v_exp_f32_e32 v8, v8
	v_max_f32_e32 v7, v7, v7
	v_med3_f32 v7, v7, s54, v223
	v_mul_f32_e32 v4, 0xbfb8aa3b, v4
	v_mul_f32_e32 v5, 0xbfb8aa3b, v5
	v_mul_f32_e32 v161, 0xbfb8aa3b, v2
	v_mul_f32_e32 v6, 0xbfb8aa3b, v6
	v_mul_f32_e32 v7, 0xbfb8aa3b, v7
	v_exp_f32_e32 v2, v4
	v_exp_f32_e32 v4, v5
	v_exp_f32_e32 v5, v161
	v_add_f32_e32 v155, 1.0, v155
	v_exp_f32_e32 v6, v6
	v_exp_f32_e32 v7, v7
	v_add_f32_e32 v8, 1.0, v8
	v_rcp_f32_e32 v155, v155
	v_rcp_f32_e32 v159, v8
	v_pk_add_f32 v[0:1], v[0:1], 1.0 op_sel_hi:[1,0]
	v_pk_add_f32 v[2:3], v[2:3], 1.0 op_sel_hi:[1,0]
	v_pk_add_f32 v[4:5], v[4:5], 1.0 op_sel_hi:[1,0]
	v_pk_add_f32 v[6:7], v[6:7], 1.0 op_sel_hi:[1,0]
	v_pk_mul_f32 v[4:5], v[4:5], v[156:157]
	v_pk_mul_f32 v[6:7], v[6:7], v[158:159]
	v_pk_mul_f32 v[2:3], v[2:3], v[154:155]
	v_pk_mul_f32 v[0:1], v[0:1], v[152:153]
